# proj K-loop: dropped per-iteration address register copies; attention main loop re-aligned to 8 bytes after the shift
# baseline (speedup 1.0000x reference)
.LBB0_497:
	s_cmpk_eq_i32 s26, 0x300
	s_cselect_b64 s[28:29], -1, 0
	s_add_i32 s23, 0, 0x10000
	s_add_i32 s30, 0, 0x14000
	ds_read_b128 v[8:11], v205
	ds_read_b128 v[12:15], v237
	ds_read_b128 v[24:27], v205 offset:2048
	ds_read_b128 v[28:31], v237 offset:2048
	ds_read_b128 v[0:3], v205 offset:16384
	ds_read_b128 v[4:7], v237 offset:16384
	ds_read_b128 v[16:19], v205 offset:18432
	ds_read_b128 v[20:23], v237 offset:18432
	s_add_i32 m0, s49, 0xc000
	s_add_u32 s30, s46, s26
	s_addc_u32 s31, s9, s27
	s_add_i32 s23, s49, 0xe000
	s_cmpk_lg_i32 s26, 0x300
	ds_read_b128 v[40:43], v239
	ds_read_b128 v[32:35], v239 offset:2048
	ds_read_b128 v[44:47], v240
	ds_read_b128 v[36:39], v240 offset:2048
	ds_read_b128 v[56:59], v239 offset:4096
	ds_read_b128 v[48:51], v239 offset:6144
	ds_read_b128 v[60:63], v240 offset:4096
	ds_read_b128 v[52:55], v240 offset:6144
	global_load_lds_dwordx4 v96, s[30:31]
	s_mov_b32 m0, s23
	s_nop 0
	global_load_lds_dwordx4 v206, s[30:31]
	s_waitcnt vmcnt(8)
	s_waitcnt lgkmcnt(0)
	s_barrier
	s_setprio 1
	s_waitcnt lgkmcnt(0)
	v_mfma_scale_f32_16x16x128_f8f6f4 v[190:193], v[8:15], v[40:47], v[190:193], v226, v225 op_sel_hi:[0,0,0]
	v_mfma_scale_f32_16x16x128_f8f6f4 v[186:189], v[24:31], v[40:47], v[186:189], v226, v225 op_sel_hi:[0,0,0]
	v_mfma_scale_f32_16x16x128_f8f6f4 v[174:177], v[8:15], v[32:39], v[174:177], v226, v225 op_sel_hi:[0,0,0]
	v_mfma_scale_f32_16x16x128_f8f6f4 v[170:173], v[24:31], v[32:39], v[170:173], v226, v225 op_sel_hi:[0,0,0]
	v_mfma_scale_f32_16x16x128_f8f6f4 v[158:161], v[8:15], v[56:63], v[158:161], v226, v225 op_sel_hi:[0,0,0]
	v_mfma_scale_f32_16x16x128_f8f6f4 v[154:157], v[24:31], v[56:63], v[154:157], v226, v225 op_sel_hi:[0,0,0]
	v_mfma_scale_f32_16x16x128_f8f6f4 v[142:145], v[8:15], v[48:55], v[142:145], v226, v225 op_sel_hi:[0,0,0]
	v_mfma_scale_f32_16x16x128_f8f6f4 v[138:141], v[24:31], v[48:55], v[138:141], v226, v225 op_sel_hi:[0,0,0]
	s_setprio 0
	s_setprio 1
	v_mfma_scale_f32_16x16x128_f8f6f4 v[182:185], v[0:7], v[40:47], v[182:185], v226, v225 op_sel_hi:[0,0,0]
	v_mfma_scale_f32_16x16x128_f8f6f4 v[178:181], v[16:23], v[40:47], v[178:181], v226, v225 op_sel_hi:[0,0,0]
	v_mfma_scale_f32_16x16x128_f8f6f4 v[166:169], v[0:7], v[32:39], v[166:169], v226, v225 op_sel_hi:[0,0,0]
	v_mfma_scale_f32_16x16x128_f8f6f4 v[162:165], v[16:23], v[32:39], v[162:165], v226, v225 op_sel_hi:[0,0,0]
	v_mfma_scale_f32_16x16x128_f8f6f4 v[150:153], v[0:7], v[56:63], v[150:153], v226, v225 op_sel_hi:[0,0,0]
	v_mfma_scale_f32_16x16x128_f8f6f4 v[146:149], v[16:23], v[56:63], v[146:149], v226, v225 op_sel_hi:[0,0,0]
	v_mfma_scale_f32_16x16x128_f8f6f4 v[134:137], v[0:7], v[48:55], v[134:137], v226, v225 op_sel_hi:[0,0,0]
	v_mfma_scale_f32_16x16x128_f8f6f4 v[130:133], v[16:23], v[48:55], v[130:133], v226, v225 op_sel_hi:[0,0,0]
	s_setprio 0
	s_barrier
	s_cbranch_scc1 .LBB0_499
	v_mov_b32_e32 v206, v210
	v_mov_b32_e32 v96, v208
	v_mov_b32_e32 v204, v243
	v_mov_b32_e32 v202, v224
	v_mov_b32_e32 v241, v210
	v_mov_b32_e32 v242, v208
	s_branch .LBB0_500
.LBB0_499:
.LBB0_500:
	s_and_b64 s[30:31], s[24:25], s[28:29]
	s_add_i32 s23, s5, 2
	s_and_b64 s[28:29], s[28:29], exec
	s_cselect_b32 s96, 0, s23
	s_and_b64 s[28:29], s[30:31], exec
	s_cselect_b32 s28, s52, s4
	s_ashr_i32 s29, s28, 31
	s_lshl_b64 s[30:31], s[96:97], 7
	s_or_b32 s96, s96, 1
	s_lshl_b64 s[34:35], s[28:29], 18
	s_lshl_b64 s[28:29], s[96:97], 7
	s_add_u32 s72, s6, s34
	s_addc_u32 s73, s7, s35
	s_add_u32 s34, s72, s30
	s_addc_u32 s35, s73, s31
	s_mov_b32 m0, s56
	ds_read_b128 v[56:59], v239 offset:16384
	ds_read_b128 v[60:63], v240 offset:16384
	ds_read_b128 v[48:51], v239 offset:18432
	ds_read_b128 v[52:55], v240 offset:18432
	ds_read_b128 v[40:43], v239 offset:20480
	ds_read_b128 v[44:47], v240 offset:20480
	ds_read_b128 v[32:35], v239 offset:22528
	ds_read_b128 v[36:39], v240 offset:22528
	global_load_lds_dwordx4 v194, s[34:35]
	s_mov_b32 m0, s57
	s_nop 0
	global_load_lds_dwordx4 v196, s[34:35]
	s_add_u32 s34, s34, 0x20000
	s_addc_u32 s35, s35, 0
	s_mov_b32 m0, s58
	s_add_u32 s30, s78, s30
	global_load_lds_dwordx4 v194, s[34:35]
	s_mov_b32 m0, s59
	s_addc_u32 s31, s79, s31
	global_load_lds_dwordx4 v196, s[34:35]
	s_mov_b32 m0, s49
	s_nop 0
	global_load_lds_dwordx4 v202, s[30:31]
	s_mov_b32 m0, s60
	s_nop 0
	global_load_lds_dwordx4 v204, s[30:31]
	s_waitcnt vmcnt(8)
	s_waitcnt lgkmcnt(0)
	s_barrier
	s_setprio 1
	s_waitcnt lgkmcnt(0)
	v_mfma_scale_f32_16x16x128_f8f6f4 v[126:129], v[8:15], v[56:63], v[126:129], v226, v225 op_sel_hi:[0,0,0]
	v_mfma_scale_f32_16x16x128_f8f6f4 v[122:125], v[24:31], v[56:63], v[122:125], v226, v225 op_sel_hi:[0,0,0]
	v_mfma_scale_f32_16x16x128_f8f6f4 v[110:113], v[8:15], v[48:55], v[110:113], v226, v225 op_sel_hi:[0,0,0]
	v_mfma_scale_f32_16x16x128_f8f6f4 v[106:109], v[24:31], v[48:55], v[106:109], v226, v225 op_sel_hi:[0,0,0]
	v_mfma_scale_f32_16x16x128_f8f6f4 v[92:95], v[8:15], v[40:47], v[92:95], v226, v225 op_sel_hi:[0,0,0]
	v_mfma_scale_f32_16x16x128_f8f6f4 v[88:91], v[24:31], v[40:47], v[88:91], v226, v225 op_sel_hi:[0,0,0]
	v_mfma_scale_f32_16x16x128_f8f6f4 v[76:79], v[8:15], v[32:39], v[76:79], v226, v225 op_sel_hi:[0,0,0]
	v_mfma_scale_f32_16x16x128_f8f6f4 v[72:75], v[24:31], v[32:39], v[72:75], v226, v225 op_sel_hi:[0,0,0]
	s_setprio 0
	s_setprio 1
	v_mfma_scale_f32_16x16x128_f8f6f4 v[118:121], v[0:7], v[56:63], v[118:121], v226, v225 op_sel_hi:[0,0,0]
	v_mfma_scale_f32_16x16x128_f8f6f4 v[114:117], v[16:23], v[56:63], v[114:117], v226, v225 op_sel_hi:[0,0,0]
	v_mfma_scale_f32_16x16x128_f8f6f4 v[102:105], v[0:7], v[48:55], v[102:105], v226, v225 op_sel_hi:[0,0,0]
	v_mfma_scale_f32_16x16x128_f8f6f4 v[98:101], v[16:23], v[48:55], v[98:101], v226, v225 op_sel_hi:[0,0,0]
	v_mfma_scale_f32_16x16x128_f8f6f4 v[84:87], v[0:7], v[40:47], v[84:87], v226, v225 op_sel_hi:[0,0,0]
	v_mfma_scale_f32_16x16x128_f8f6f4 v[80:83], v[16:23], v[40:47], v[80:83], v226, v225 op_sel_hi:[0,0,0]
	v_mfma_scale_f32_16x16x128_f8f6f4 v[68:71], v[0:7], v[32:39], v[68:71], v226, v225 op_sel_hi:[0,0,0]
	v_mfma_scale_f32_16x16x128_f8f6f4 v[64:67], v[16:23], v[32:39], v[64:67], v226, v225 op_sel_hi:[0,0,0]
	s_setprio 0
	s_barrier
	s_add_i32 s34, 0, 0x18000
	s_add_i32 s35, 0, 0x1c000
	ds_read_b128 v[0:3], v205 offset:32768
	ds_read_b128 v[4:7], v237 offset:32768
	ds_read_b128 v[8:11], v205 offset:34816
	ds_read_b128 v[12:15], v237 offset:34816
	ds_read_b128 v[16:19], v205 offset:49152
	ds_read_b128 v[20:23], v237 offset:49152
	ds_read_b128 v[24:27], v205 offset:51200
	ds_read_b128 v[28:31], v237 offset:51200
	s_mov_b32 m0, s61
	ds_read_b128 v[32:35], v239 offset:32768
	ds_read_b128 v[40:43], v239 offset:34816
	ds_read_b128 v[36:39], v240 offset:32768
	ds_read_b128 v[44:47], v240 offset:34816
	ds_read_b128 v[48:51], v239 offset:36864
	ds_read_b128 v[56:59], v239 offset:38912
	ds_read_b128 v[52:55], v240 offset:36864
	ds_read_b128 v[60:63], v240 offset:38912
	global_load_lds_dwordx4 v96, s[30:31]
	s_mov_b32 m0, s64
	s_nop 0
	global_load_lds_dwordx4 v206, s[30:31]
	s_waitcnt vmcnt(8)
	s_waitcnt lgkmcnt(0)
	s_barrier
	s_setprio 1
	s_waitcnt lgkmcnt(0)
	v_mfma_scale_f32_16x16x128_f8f6f4 v[190:193], v[0:7], v[32:39], v[190:193], v226, v225 op_sel_hi:[0,0,0]
	v_mfma_scale_f32_16x16x128_f8f6f4 v[186:189], v[8:15], v[32:39], v[186:189], v226, v225 op_sel_hi:[0,0,0]
	v_mfma_scale_f32_16x16x128_f8f6f4 v[174:177], v[0:7], v[40:47], v[174:177], v226, v225 op_sel_hi:[0,0,0]
	v_mfma_scale_f32_16x16x128_f8f6f4 v[170:173], v[8:15], v[40:47], v[170:173], v226, v225 op_sel_hi:[0,0,0]
	v_mfma_scale_f32_16x16x128_f8f6f4 v[158:161], v[0:7], v[48:55], v[158:161], v226, v225 op_sel_hi:[0,0,0]
	v_mfma_scale_f32_16x16x128_f8f6f4 v[154:157], v[8:15], v[48:55], v[154:157], v226, v225 op_sel_hi:[0,0,0]
	v_mfma_scale_f32_16x16x128_f8f6f4 v[142:145], v[0:7], v[56:63], v[142:145], v226, v225 op_sel_hi:[0,0,0]
	v_mfma_scale_f32_16x16x128_f8f6f4 v[138:141], v[8:15], v[56:63], v[138:141], v226, v225 op_sel_hi:[0,0,0]
	s_setprio 0
	s_setprio 1
	v_mfma_scale_f32_16x16x128_f8f6f4 v[182:185], v[16:23], v[32:39], v[182:185], v226, v225 op_sel_hi:[0,0,0]
	v_mfma_scale_f32_16x16x128_f8f6f4 v[178:181], v[24:31], v[32:39], v[178:181], v226, v225 op_sel_hi:[0,0,0]
	v_mfma_scale_f32_16x16x128_f8f6f4 v[166:169], v[16:23], v[40:47], v[166:169], v226, v225 op_sel_hi:[0,0,0]
	v_mfma_scale_f32_16x16x128_f8f6f4 v[162:165], v[24:31], v[40:47], v[162:165], v226, v225 op_sel_hi:[0,0,0]
	v_mfma_scale_f32_16x16x128_f8f6f4 v[150:153], v[16:23], v[48:55], v[150:153], v226, v225 op_sel_hi:[0,0,0]
	v_mfma_scale_f32_16x16x128_f8f6f4 v[146:149], v[24:31], v[48:55], v[146:149], v226, v225 op_sel_hi:[0,0,0]
	v_mfma_scale_f32_16x16x128_f8f6f4 v[134:137], v[16:23], v[56:63], v[134:137], v226, v225 op_sel_hi:[0,0,0]
	v_mfma_scale_f32_16x16x128_f8f6f4 v[130:133], v[24:31], v[56:63], v[130:133], v226, v225 op_sel_hi:[0,0,0]
	s_setprio 0
	s_barrier
	s_add_u32 s30, s72, s28
	s_addc_u32 s31, s73, s29
	s_add_i32 s34, s34, s48
	s_mov_b32 m0, s34
	ds_read_b128 v[32:35], v239 offset:49152
	ds_read_b128 v[40:43], v239 offset:51200
	ds_read_b128 v[36:39], v240 offset:49152
	ds_read_b128 v[44:47], v240 offset:51200
	ds_read_b128 v[48:51], v239 offset:53248
	ds_read_b128 v[56:59], v239 offset:55296
	ds_read_b128 v[52:55], v240 offset:53248
	ds_read_b128 v[60:63], v240 offset:55296
	global_load_lds_dwordx4 v194, s[30:31]
	s_add_i32 m0, s34, 0x2000
	s_add_i32 s34, s35, s48
	global_load_lds_dwordx4 v196, s[30:31]
	s_add_u32 s30, s30, 0x20000
	s_addc_u32 s31, s31, 0
	s_mov_b32 m0, s34
	s_nop 0
	global_load_lds_dwordx4 v194, s[30:31]
	s_add_i32 m0, s34, 0x2000
	s_add_u32 s28, s78, s28
	global_load_lds_dwordx4 v196, s[30:31]
	s_addc_u32 s29, s79, s29
	s_mov_b32 m0, s65
	s_nop 0
	global_load_lds_dwordx4 v202, s[28:29]
	s_mov_b32 m0, s92
	s_nop 0
	global_load_lds_dwordx4 v204, s[28:29]
	s_waitcnt vmcnt(8)
	s_waitcnt lgkmcnt(0)
	s_barrier
	s_setprio 1
	s_waitcnt lgkmcnt(0)
	v_mfma_scale_f32_16x16x128_f8f6f4 v[126:129], v[0:7], v[32:39], v[126:129], v226, v225 op_sel_hi:[0,0,0]
	v_mfma_scale_f32_16x16x128_f8f6f4 v[122:125], v[8:15], v[32:39], v[122:125], v226, v225 op_sel_hi:[0,0,0]
	v_mfma_scale_f32_16x16x128_f8f6f4 v[110:113], v[0:7], v[40:47], v[110:113], v226, v225 op_sel_hi:[0,0,0]
	v_mfma_scale_f32_16x16x128_f8f6f4 v[106:109], v[8:15], v[40:47], v[106:109], v226, v225 op_sel_hi:[0,0,0]
	v_mfma_scale_f32_16x16x128_f8f6f4 v[92:95], v[0:7], v[48:55], v[92:95], v226, v225 op_sel_hi:[0,0,0]
	v_mfma_scale_f32_16x16x128_f8f6f4 v[88:91], v[8:15], v[48:55], v[88:91], v226, v225 op_sel_hi:[0,0,0]
	v_mfma_scale_f32_16x16x128_f8f6f4 v[76:79], v[0:7], v[56:63], v[76:79], v226, v225 op_sel_hi:[0,0,0]
	v_mfma_scale_f32_16x16x128_f8f6f4 v[72:75], v[8:15], v[56:63], v[72:75], v226, v225 op_sel_hi:[0,0,0]
	s_setprio 0
	s_setprio 1
	v_mfma_scale_f32_16x16x128_f8f6f4 v[118:121], v[16:23], v[32:39], v[118:121], v226, v225 op_sel_hi:[0,0,0]
	v_mfma_scale_f32_16x16x128_f8f6f4 v[114:117], v[24:31], v[32:39], v[114:117], v226, v225 op_sel_hi:[0,0,0]
	v_mfma_scale_f32_16x16x128_f8f6f4 v[102:105], v[16:23], v[40:47], v[102:105], v226, v225 op_sel_hi:[0,0,0]
	v_mfma_scale_f32_16x16x128_f8f6f4 v[98:101], v[24:31], v[40:47], v[98:101], v226, v225 op_sel_hi:[0,0,0]
	v_mfma_scale_f32_16x16x128_f8f6f4 v[84:87], v[16:23], v[48:55], v[84:87], v226, v225 op_sel_hi:[0,0,0]
	v_mfma_scale_f32_16x16x128_f8f6f4 v[80:83], v[24:31], v[48:55], v[80:83], v226, v225 op_sel_hi:[0,0,0]
	v_mfma_scale_f32_16x16x128_f8f6f4 v[68:71], v[16:23], v[56:63], v[68:71], v226, v225 op_sel_hi:[0,0,0]
	v_mfma_scale_f32_16x16x128_f8f6f4 v[64:67], v[24:31], v[56:63], v[64:67], v226, v225 op_sel_hi:[0,0,0]
	s_setprio 0
	s_barrier
	s_add_u32 s26, s26, 0x100
	s_addc_u32 s27, s27, 0
	s_cmp_gt_u32 s5, 5
	s_cbranch_scc1 .LBB0_502
	s_mov_b32 s5, s23
	s_branch .LBB0_497

.LBB0_724:
	v_lshlrev_b32_e32 v32, 1, v118
	v_and_b32_e32 v218, 32, v32
	v_lshrrev_b32_e32 v32, 2, v118
	v_and_or_b32 v32, v32, 3, v236
	v_lshlrev_b32_e32 v217, 6, v32
	v_add_u32_e32 v32, 0, v218
	v_add3_u32 v239, v32, v216, v217
	v_max3_f32 v32, v16, v17, v0
	v_max3_f32 v33, v18, v19, v1
	s_and_b32 s19, s41, 0x3fffffc0
	v_max3_f32 v32, v32, v2, v3
	v_max3_f32 v33, v33, v22, v23
	s_add_i32 s20, s45, 0x100
	v_max3_f32 v32, v32, v20, v21
	v_max3_f32 v33, v33, v6, v7
	s_lshl_b32 s19, s19, 2
	v_max3_f32 v32, v32, v4, v5
	v_max3_f32 v33, v33, v26, v27
	s_lshr_b32 s39, s20, 6
	v_max3_f32 v32, v32, v24, v25
	v_max3_f32 v33, v33, v10, v11
	s_mov_b64 s[20:21], 0x60000
	v_max3_f32 v32, v32, v8, v9
	v_max3_f32 v33, v33, v30, v31
	s_add_i32 s19, s19, 0
	v_max3_f32 v32, v32, v28, v29
	v_max3_f32 v33, v33, v14, v15
	s_cmp_lg_u32 0, -1
	v_max3_f32 v32, v32, v12, v13
	s_mov_b32 s96, 1
	v_max_f32_e32 v32, v32, v33
	s_mov_b32 s22, 0
	v_mov_b32_e32 v33, v32
	s_nop 1
	v_permlane32_swap_b32_e32 v32, v33
	v_max_f32_e32 v32, v32, v33
	v_lshl_add_u32 v235, v214, 2, s19
	v_sub_f32_e32 v64, v0, v32
	v_sub_f32_e32 v0, v17, v32
	v_sub_f32_e32 v16, v16, v32
	v_sub_f32_e32 v65, v1, v32
	v_sub_f32_e32 v1, v18, v32
	v_sub_f32_e32 v66, v2, v32
	v_sub_f32_e32 v2, v19, v32
	s_nop 0
	v_exp_f32_e32 v81, v0
	v_lshl_add_u32 v0, v236, 2, 0
	v_sub_f32_e32 v67, v3, v32
	v_sub_f32_e32 v3, v20, v32
	v_sub_f32_e32 v68, v4, v32
	v_sub_f32_e32 v4, v21, v32
	v_sub_f32_e32 v69, v5, v32
	v_sub_f32_e32 v5, v22, v32
	v_sub_f32_e32 v70, v6, v32
	v_sub_f32_e32 v6, v23, v32
	v_sub_f32_e32 v71, v7, v32
	v_sub_f32_e32 v7, v24, v32
	v_sub_f32_e32 v72, v8, v32
	v_sub_f32_e32 v8, v25, v32
	v_sub_f32_e32 v73, v9, v32
	v_sub_f32_e32 v9, v26, v32
	v_sub_f32_e32 v74, v10, v32
	v_sub_f32_e32 v10, v27, v32
	v_sub_f32_e32 v75, v11, v32
	v_sub_f32_e32 v11, v28, v32
	v_sub_f32_e32 v76, v12, v32
	v_sub_f32_e32 v12, v29, v32
	v_sub_f32_e32 v77, v13, v32
	v_sub_f32_e32 v13, v30, v32
	v_sub_f32_e32 v78, v14, v32
	v_sub_f32_e32 v14, v31, v32
	v_add_u32_e32 v28, 0x15100, v0
	v_sub_f32_e32 v79, v15, v32
	v_exp_f32_e32 v80, v16
	v_exp_f32_e32 v82, v1
	v_exp_f32_e32 v83, v2
	v_exp_f32_e32 v84, v3
	v_exp_f32_e32 v85, v4
	v_exp_f32_e32 v86, v5
	v_exp_f32_e32 v87, v6
	v_exp_f32_e32 v88, v7
	v_exp_f32_e32 v89, v8
	v_exp_f32_e32 v90, v9
	v_exp_f32_e32 v91, v10
	v_exp_f32_e32 v92, v11
	v_exp_f32_e32 v93, v12
	v_exp_f32_e32 v94, v13
	v_exp_f32_e32 v95, v14
	ds_read_b128 v[0:3], v28
	ds_read_b128 v[4:7], v28 offset:32
	ds_read_b128 v[8:11], v28 offset:128
	ds_read_b128 v[12:15], v28 offset:160
	ds_read_b128 v[16:19], v28 offset:64
	ds_read_b128 v[20:23], v28 offset:96
	ds_read_b128 v[24:27], v28 offset:192
	ds_read_b128 v[28:31], v28 offset:224
	s_waitcnt vmcnt(0) lgkmcnt(0)
	s_barrier
	v_add_f32_e32 v202, v97, v32
	v_exp_f32_e32 v64, v64
	s_waitcnt lgkmcnt(7)
	v_pk_add_f32 v[48:49], v[202:203], v[0:1] op_sel_hi:[0,1] neg_lo:[1,0] neg_hi:[1,0]
	v_lshl_add_u64 v[0:1], v[114:115], 0, s[20:21]
	s_mov_b32 s20, m0
	s_mov_b32 m0, s30
	s_nop 0
	global_load_lds_dwordx4 v[0:1], off
	s_mov_b32 m0, s20
	s_mov_b64 s[20:21], 0x20000
	v_lshl_add_u64 v[0:1], v[116:117], 0, s[20:21]
	s_cselect_b32 s20, 0, 0
	s_add_i32 s18, s20, s18
	s_add_i32 s18, s18, 0x8000
	s_mov_b32 s20, m0
	s_mov_b32 m0, s18
	s_nop 0
	global_load_lds_dwordx4 v[0:1], off
	s_mov_b32 m0, s20
	ds_read_b128 v[158:161], v238 offset:8192
	ds_read_b128 v[146:149], v238 offset:8704
	ds_read_b128 v[154:157], v238 offset:10240
	ds_read_b128 v[142:145], v238 offset:10752
	ds_read_b128 v[150:153], v238 offset:12288
	ds_read_b128 v[138:141], v238 offset:12800
	ds_read_b128 v[134:137], v238 offset:14336
	ds_read_b128 v[130:133], v238 offset:14848
	v_exp_f32_e32 v65, v65
	v_exp_f32_e32 v66, v66
	v_exp_f32_e32 v67, v67
	v_exp_f32_e32 v68, v68
	v_exp_f32_e32 v69, v69
	v_exp_f32_e32 v70, v70
	v_exp_f32_e32 v71, v71
	v_exp_f32_e32 v72, v72
	v_exp_f32_e32 v73, v73
	v_exp_f32_e32 v74, v74
	v_exp_f32_e32 v75, v75
	v_exp_f32_e32 v76, v76
	v_exp_f32_e32 v77, v77
	v_exp_f32_e32 v78, v78
	v_exp_f32_e32 v79, v79
	s_waitcnt vmcnt(2) lgkmcnt(0)
	s_barrier
	v_and_b32_e32 v0, 3, v118
	s_waitcnt lgkmcnt(13)
	v_pk_add_f32 v[32:33], v[202:203], v[8:9] op_sel_hi:[0,1] neg_lo:[1,0] neg_hi:[1,0]
	v_pk_add_f32 v[50:51], v[202:203], v[2:3] op_sel_hi:[0,1] neg_lo:[1,0] neg_hi:[1,0]
	v_pk_add_f32 v[34:35], v[202:203], v[10:11] op_sel_hi:[0,1] neg_lo:[1,0] neg_hi:[1,0]
	v_pk_add_f32 v[52:53], v[202:203], v[4:5] op_sel_hi:[0,1] neg_lo:[1,0] neg_hi:[1,0]
	s_waitcnt lgkmcnt(12)
	v_pk_add_f32 v[36:37], v[202:203], v[12:13] op_sel_hi:[0,1] neg_lo:[1,0] neg_hi:[1,0]
	v_pk_add_f32 v[54:55], v[202:203], v[6:7] op_sel_hi:[0,1] neg_lo:[1,0] neg_hi:[1,0]
	v_pk_add_f32 v[38:39], v[202:203], v[14:15] op_sel_hi:[0,1] neg_lo:[1,0] neg_hi:[1,0]
	s_waitcnt lgkmcnt(11)
	v_pk_add_f32 v[56:57], v[202:203], v[16:17] op_sel_hi:[0,1] neg_lo:[1,0] neg_hi:[1,0]
	s_waitcnt lgkmcnt(9)
	v_pk_add_f32 v[40:41], v[202:203], v[24:25] op_sel_hi:[0,1] neg_lo:[1,0] neg_hi:[1,0]
	v_pk_add_f32 v[58:59], v[202:203], v[18:19] op_sel_hi:[0,1] neg_lo:[1,0] neg_hi:[1,0]
	v_pk_add_f32 v[42:43], v[202:203], v[26:27] op_sel_hi:[0,1] neg_lo:[1,0] neg_hi:[1,0]
	v_pk_add_f32 v[60:61], v[202:203], v[20:21] op_sel_hi:[0,1] neg_lo:[1,0] neg_hi:[1,0]
	s_waitcnt lgkmcnt(8)
	v_pk_add_f32 v[44:45], v[202:203], v[28:29] op_sel_hi:[0,1] neg_lo:[1,0] neg_hi:[1,0]
	v_pk_add_f32 v[62:63], v[202:203], v[22:23] op_sel_hi:[0,1] neg_lo:[1,0] neg_hi:[1,0]
	v_pk_add_f32 v[46:47], v[202:203], v[30:31] op_sel_hi:[0,1] neg_lo:[1,0] neg_hi:[1,0]
	s_andn2_b64 vcc, exec, s[2:3]
	v_cmp_gt_u32_e64 s[2:3], 32, v199
	v_lshl_add_u32 v219, v236, 2, s19
	v_lshlrev_b32_e32 v204, 4, v0
	s_cbranch_vccnz .LBB0_742
	s_lshl_b64 s[18:19], s[4:5], 1
	s_add_u32 s18, s70, s18
	s_addc_u32 s19, s71, s19
	s_add_u32 s18, s18, s14
	s_addc_u32 s19, s19, s15
	v_lshl_add_u64 v[206:207], s[18:19], 0, v[96:97]
	s_lshl_b64 s[18:19], s[16:17], 1
	s_add_u32 s18, s18, s14
	v_mov_b32_e32 v205, v97
	s_addc_u32 s19, s19, s15
	v_lshl_add_u64 v[0:1], s[18:19], 0, v[204:205]
	s_lshl_b32 s18, s41, 9
	s_and_b32 s18, s18, 0x18000
	v_lshl_or_b32 v2, v241, 11, s18
	v_mov_b32_e32 v3, v97
	v_lshl_add_u64 v[0:1], v[0:1], 0, v[2:3]
	v_mov_b32_e32 v16, v97
	v_mov_b32_e32 v17, v97
	v_lshl_add_u64 v[208:209], s[70:71], 0, v[0:1]
	v_subrev_u32_e32 v245, s14, v0
	v_add_u32_e32 v245, 0x7fc0000, v245
	v_lshl_add_u32 v244, s4, 1, v96
	s_add_u32 s98, s70, s14
	s_addc_u32 s99, s71, s15
	s_add_u32 s98, s98, s12
	s_addc_u32 s99, s99, s13
	s_add_u32 s98, s98, 0x16e80000
	s_addc_u32 s99, s99, 0
	v_readlane_b32 s18, v253, 11
	v_mov_b32_e32 v18, v97
	v_mov_b32_e32 v19, v97
	v_mov_b32_e32 v20, v97
	v_mov_b32_e32 v21, v97
	v_mov_b32_e32 v22, v97
	v_mov_b32_e32 v23, v97
	v_mov_b32_e32 v24, v97
	v_mov_b32_e32 v25, v97
	v_mov_b32_e32 v26, v97
	v_mov_b32_e32 v27, v97
	v_mov_b32_e32 v28, v97
	v_mov_b32_e32 v29, v97
	v_mov_b32_e32 v30, v97
	v_mov_b32_e32 v31, v97
	v_mov_b64_e32 v[0:1], v[16:17]
	v_lshl_add_u32 v205, v215, 4, s18
	s_mov_b32 s18, 0
	s_movk_i32 s22, 0x4000
	s_movk_i32 s38, 0x2000
	v_mov_b32_e32 v240, 0
	s_mov_b32 s23, 6
	v_mov_b64_e32 v[2:3], v[18:19]
	v_mov_b64_e32 v[4:5], v[20:21]
	v_mov_b64_e32 v[6:7], v[22:23]
	v_mov_b64_e32 v[8:9], v[24:25]
	v_mov_b64_e32 v[10:11], v[26:27]
	v_mov_b64_e32 v[12:13], v[28:29]
	v_mov_b64_e32 v[14:15], v[30:31]
	s_nop 0
	s_nop 0
